# FoX tile loop: tiles that do not touch the causal diagonal (wave-uniform flag clear) take a copy of the score section without the key-index / compare / select work (masks are all zero there, selects k
# speedup vs baseline: 1.0077x; 1.0048x over previous
.LBB0_651:
	s_cmp_gt_i32 s8, s59
	s_cbranch_scc1 .LBB0_656
	s_bitcmp1_b32 s8, 0
	s_cselect_b32 s8, 0x8100, 0
	s_add_i32 s61, s8, 0
	v_mov_b32_e32 v2, v146
	v_add_u32_e32 v12, s61, v178
	v_lshl_add_u32 v192, v151, 2, s61
	v_xad_u32 v8, v2, v148, v12
	ds_read_b128 v[4:7], v8 offset:16384
	ds_read_b128 v[8:11], v8 offset:24576
	s_waitcnt lgkmcnt(0)
	v_mfma_f32_32x32x16_bf16 v[82:97], v[4:7], v[114:117], 0
	v_xad_u32 v13, v2, v177, v12
	s_add_i32 s8, s16, -1
	s_cmp_gt_i32 s8, s49
	v_mfma_f32_32x32x16_bf16 v[98:113], v[8:11], v[114:117], 0
	ds_read_b128 v[4:7], v13 offset:16384
	ds_read_b128 v[8:11], v13 offset:24576
	v_xad_u32 v13, v2, v176, v12
	s_waitcnt lgkmcnt(0)
	v_mfma_f32_32x32x16_bf16 v[82:97], v[4:7], v[118:121], v[82:97]
	v_mfma_f32_32x32x16_bf16 v[98:113], v[8:11], v[118:121], v[98:113]
	ds_read_b128 v[4:7], v13 offset:16384
	ds_read_b128 v[8:11], v13 offset:24576
	v_xad_u32 v13, v2, v175, v12
	s_waitcnt lgkmcnt(0)
	v_mfma_f32_32x32x16_bf16 v[82:97], v[4:7], v[122:125], v[82:97]
	v_mfma_f32_32x32x16_bf16 v[98:113], v[8:11], v[122:125], v[98:113]
	ds_read_b128 v[4:7], v13 offset:16384
	ds_read_b128 v[8:11], v13 offset:24576
	v_xad_u32 v13, v2, v174, v12
	s_waitcnt lgkmcnt(0)
	v_mfma_f32_32x32x16_bf16 v[82:97], v[4:7], v[126:129], v[82:97]
	v_mfma_f32_32x32x16_bf16 v[98:113], v[8:11], v[126:129], v[98:113]
	ds_read_b128 v[4:7], v13 offset:16384
	ds_read_b128 v[8:11], v13 offset:24576
	v_xad_u32 v13, v2, v173, v12
	s_waitcnt lgkmcnt(0)
	v_mfma_f32_32x32x16_bf16 v[82:97], v[4:7], v[130:133], v[82:97]
	v_mfma_f32_32x32x16_bf16 v[98:113], v[8:11], v[130:133], v[98:113]
	ds_read_b128 v[4:7], v13 offset:16384
	ds_read_b128 v[8:11], v13 offset:24576
	v_xad_u32 v13, v2, v172, v12
	v_xad_u32 v2, v2, v171, v12
	s_waitcnt lgkmcnt(0)
	v_mfma_f32_32x32x16_bf16 v[82:97], v[4:7], v[134:137], v[82:97]
	v_mfma_f32_32x32x16_bf16 v[98:113], v[8:11], v[134:137], v[98:113]
	ds_read_b128 v[4:7], v13 offset:16384
	ds_read_b128 v[8:11], v13 offset:24576
	s_waitcnt lgkmcnt(0)
	v_mfma_f32_32x32x16_bf16 v[82:97], v[4:7], v[138:141], v[82:97]
	v_mfma_f32_32x32x16_bf16 v[98:113], v[8:11], v[138:141], v[98:113]
	ds_read_b128 v[4:7], v2 offset:16384
	ds_read_b128 v[8:11], v2 offset:24576
	ds_read_b128 v[12:15], v192 offset:32768
	ds_read_b128 v[184:187], v192 offset:32800
	ds_read_b128 v[180:183], v192 offset:32896
	ds_read_b128 v[188:191], v192 offset:32928
	s_waitcnt lgkmcnt(0)
	v_mfma_f32_32x32x16_bf16 v[82:97], v[4:7], v[142:145], v[82:97]
	v_add_u32_e32 v4, s16, v151
	v_subrev_u32_e32 v7, 32, v4
	v_subrev_u32_e32 v2, 64, v4
	v_cmp_gt_i32_e64 s[10:11], v7, v150
	v_cmp_lt_i32_e32 vcc, v2, v150
	v_cmp_gt_i32_e64 s[8:9], v2, v150
	s_nop 5
	v_fmamk_f32 v7, v83, 0x3fb8aa3b, v170
	v_mfma_f32_32x32x16_bf16 v[98:113], v[8:11], v[142:145], v[98:113]
	v_fmac_f32_e32 v7, 0xbfb8aa3b, v13
	v_fmamk_f32 v6, v82, 0x3fb8aa3b, v170
	v_cndmask_b32_e32 v2, v165, v7, vcc
	s_cselect_b64 vcc, -1, 0
	s_cbranch_scc0 .Lfox_nomask
	v_fmac_f32_e32 v6, 0xbfb8aa3b, v12
	s_and_b64 s[8:9], vcc, s[8:9]
	v_subrev_u32_e32 v9, 31, v4
	s_nop 4
	v_fmamk_f32 v5, v98, 0x3fb8aa3b, v170
	v_cndmask_b32_e32 v2, v7, v2, vcc
	v_cndmask_b32_e64 v6, v6, v165, s[8:9]
	v_fmamk_f32 v7, v99, 0x3fb8aa3b, v170
	v_cmp_gt_i32_e64 s[8:9], v9, v150
	v_fmac_f32_e32 v5, 0xbfb8aa3b, v180
	s_and_b64 s[10:11], vcc, s[10:11]
	v_fmac_f32_e32 v7, 0xbfb8aa3b, v181
	s_and_b64 s[8:9], vcc, s[8:9]
	v_cndmask_b32_e64 v5, v5, v165, s[10:11]
	v_cndmask_b32_e64 v7, v7, v165, s[8:9]
	v_max_f32_e32 v8, v6, v5
	v_max_f32_e32 v9, v2, v7
	v_subrev_u32_e32 v10, 62, v4
	v_max3_f32 v12, v8, s45, v9
	v_fmamk_f32 v9, v84, 0x3fb8aa3b, v170
	v_cmp_gt_i32_e64 s[8:9], v10, v150
	v_subrev_u32_e32 v10, 30, v4
	v_fmac_f32_e32 v9, 0xbfb8aa3b, v14
	v_fmamk_f32 v8, v100, 0x3fb8aa3b, v170
	v_cmp_gt_i32_e64 s[10:11], v10, v150
	s_and_b64 s[8:9], vcc, s[8:9]
	v_subrev_u32_e32 v14, 61, v4
	v_fmac_f32_e32 v8, 0xbfb8aa3b, v182
	s_and_b64 s[10:11], vcc, s[10:11]
	v_cndmask_b32_e64 v9, v9, v165, s[8:9]
	v_cmp_gt_i32_e64 s[8:9], v14, v150
	v_subrev_u32_e32 v14, 29, v4
	v_cndmask_b32_e64 v8, v8, v165, s[10:11]
	v_fmamk_f32 v11, v85, 0x3fb8aa3b, v170
	v_fmamk_f32 v10, v101, 0x3fb8aa3b, v170
	v_cmp_gt_i32_e64 s[10:11], v14, v150
	v_fmac_f32_e32 v11, 0xbfb8aa3b, v15
	v_fmac_f32_e32 v10, 0xbfb8aa3b, v183
	s_and_b64 s[10:11], vcc, s[10:11]
	s_and_b64 s[8:9], vcc, s[8:9]
	v_cndmask_b32_e64 v10, v10, v165, s[10:11]
	v_cndmask_b32_e64 v11, v11, v165, s[8:9]
	v_max_f32_e32 v13, v9, v8
	v_max_f32_e32 v14, v11, v10
	v_max3_f32 v16, v12, v13, v14
	v_subrev_u32_e32 v14, 56, v4
	v_fmamk_f32 v13, v86, 0x3fb8aa3b, v170
	v_cmp_gt_i32_e64 s[8:9], v14, v150
	v_subrev_u32_e32 v14, 24, v4
	v_fmac_f32_e32 v13, 0xbfb8aa3b, v184
	v_fmamk_f32 v12, v102, 0x3fb8aa3b, v170
	v_cmp_gt_i32_e64 s[10:11], v14, v150
	s_and_b64 s[8:9], vcc, s[8:9]
	v_subrev_u32_e32 v82, 55, v4
	v_fmac_f32_e32 v12, 0xbfb8aa3b, v188
	s_and_b64 s[10:11], vcc, s[10:11]
	v_cndmask_b32_e64 v13, v13, v165, s[8:9]
	v_cmp_gt_i32_e64 s[8:9], v82, v150
	v_subrev_u32_e32 v82, 23, v4
	v_cndmask_b32_e64 v12, v12, v165, s[10:11]
	v_fmamk_f32 v15, v87, 0x3fb8aa3b, v170
	v_fmamk_f32 v14, v103, 0x3fb8aa3b, v170
	v_cmp_gt_i32_e64 s[10:11], v82, v150
	v_fmac_f32_e32 v15, 0xbfb8aa3b, v185
	v_fmac_f32_e32 v14, 0xbfb8aa3b, v189
	s_and_b64 s[10:11], vcc, s[10:11]
	s_and_b64 s[8:9], vcc, s[8:9]
	v_cndmask_b32_e64 v14, v14, v165, s[10:11]
	v_cndmask_b32_e64 v15, v15, v165, s[8:9]
	v_max_f32_e32 v17, v13, v12
	v_max_f32_e32 v82, v15, v14
	v_max3_f32 v84, v16, v17, v82
	v_subrev_u32_e32 v82, 54, v4
	v_fmamk_f32 v17, v88, 0x3fb8aa3b, v170
	v_cmp_gt_i32_e64 s[8:9], v82, v150
	v_subrev_u32_e32 v82, 22, v4
	v_fmac_f32_e32 v17, 0xbfb8aa3b, v186
	v_fmamk_f32 v16, v104, 0x3fb8aa3b, v170
	v_cmp_gt_i32_e64 s[10:11], v82, v150
	s_and_b64 s[8:9], vcc, s[8:9]
	v_subrev_u32_e32 v86, 53, v4
	v_fmac_f32_e32 v16, 0xbfb8aa3b, v190
	s_and_b64 s[10:11], vcc, s[10:11]
	v_cndmask_b32_e64 v17, v17, v165, s[8:9]
	v_cmp_gt_i32_e64 s[8:9], v86, v150
	v_subrev_u32_e32 v86, 21, v4
	v_cndmask_b32_e64 v16, v16, v165, s[10:11]
	v_fmamk_f32 v83, v89, 0x3fb8aa3b, v170
	v_fmamk_f32 v82, v105, 0x3fb8aa3b, v170
	v_cmp_gt_i32_e64 s[10:11], v86, v150
	v_fmac_f32_e32 v83, 0xbfb8aa3b, v187
	v_fmac_f32_e32 v82, 0xbfb8aa3b, v191
	s_and_b64 s[10:11], vcc, s[10:11]
	s_and_b64 s[8:9], vcc, s[8:9]
	ds_read_b128 v[98:101], v192 offset:32832
	ds_read_b128 v[180:183], v192 offset:32864
	v_cndmask_b32_e64 v82, v82, v165, s[10:11]
	v_cndmask_b32_e64 v83, v83, v165, s[8:9]
	ds_read_b128 v[102:105], v192 offset:32960
	ds_read_b128 v[184:187], v192 offset:32992
	v_max_f32_e32 v85, v17, v16
	v_max_f32_e32 v86, v83, v82
	v_max3_f32 v87, v84, v85, v86
	v_subrev_u32_e32 v86, 48, v4
	v_fmamk_f32 v85, v90, 0x3fb8aa3b, v170
	v_cmp_gt_i32_e64 s[8:9], v86, v150
	v_add_u32_e32 v86, -16, v4
	s_waitcnt lgkmcnt(0)
	v_fmac_f32_e32 v85, 0xbfb8aa3b, v98
	v_fmamk_f32 v84, v106, 0x3fb8aa3b, v170
	v_cmp_gt_i32_e64 s[10:11], v86, v150
	s_and_b64 s[8:9], vcc, s[8:9]
	v_subrev_u32_e32 v90, 47, v4
	v_fmac_f32_e32 v84, 0xbfb8aa3b, v102
	s_and_b64 s[10:11], vcc, s[10:11]
	v_cndmask_b32_e64 v85, v85, v165, s[8:9]
	v_cmp_gt_i32_e64 s[8:9], v90, v150
	v_add_u32_e32 v90, -15, v4
	v_cndmask_b32_e64 v84, v84, v165, s[10:11]
	v_fmamk_f32 v88, v91, 0x3fb8aa3b, v170
	v_fmamk_f32 v86, v107, 0x3fb8aa3b, v170
	v_cmp_gt_i32_e64 s[10:11], v90, v150
	v_fmac_f32_e32 v88, 0xbfb8aa3b, v99
	v_fmac_f32_e32 v86, 0xbfb8aa3b, v103
	s_and_b64 s[10:11], vcc, s[10:11]
	s_and_b64 s[8:9], vcc, s[8:9]
	v_cndmask_b32_e64 v86, v86, v165, s[10:11]
	v_cndmask_b32_e64 v88, v88, v165, s[8:9]
	v_max_f32_e32 v89, v85, v84
	v_max_f32_e32 v90, v88, v86
	v_max3_f32 v98, v87, v89, v90
	v_subrev_u32_e32 v90, 46, v4
	v_fmamk_f32 v89, v92, 0x3fb8aa3b, v170
	v_cmp_gt_i32_e64 s[8:9], v90, v150
	v_add_u32_e32 v90, -14, v4
	v_fmac_f32_e32 v89, 0xbfb8aa3b, v100
	v_fmamk_f32 v87, v108, 0x3fb8aa3b, v170
	v_cmp_gt_i32_e64 s[10:11], v90, v150
	s_and_b64 s[8:9], vcc, s[8:9]
	v_fmamk_f32 v91, v93, 0x3fb8aa3b, v170
	v_subrev_u32_e32 v93, 45, v4
	v_fmac_f32_e32 v87, 0xbfb8aa3b, v104
	s_and_b64 s[10:11], vcc, s[10:11]
	v_cndmask_b32_e64 v89, v89, v165, s[8:9]
	v_cmp_gt_i32_e64 s[8:9], v93, v150
	v_add_u32_e32 v93, -13, v4
	v_cndmask_b32_e64 v87, v87, v165, s[10:11]
	v_fmamk_f32 v90, v109, 0x3fb8aa3b, v170
	v_cmp_gt_i32_e64 s[10:11], v93, v150
	v_fmac_f32_e32 v91, 0xbfb8aa3b, v101
	v_fmac_f32_e32 v90, 0xbfb8aa3b, v105
	s_and_b64 s[10:11], vcc, s[10:11]
	s_and_b64 s[8:9], vcc, s[8:9]
	v_cndmask_b32_e64 v90, v90, v165, s[10:11]
	v_cndmask_b32_e64 v91, v91, v165, s[8:9]
	v_max_f32_e32 v92, v89, v87
	v_max_f32_e32 v93, v91, v90
	v_max3_f32 v98, v98, v92, v93
	v_fmamk_f32 v93, v94, 0x3fb8aa3b, v170
	v_subrev_u32_e32 v94, 40, v4
	v_cmp_gt_i32_e64 s[8:9], v94, v150
	v_add_u32_e32 v94, -8, v4
	v_fmac_f32_e32 v93, 0xbfb8aa3b, v180
	v_fmamk_f32 v92, v110, 0x3fb8aa3b, v170
	v_cmp_gt_i32_e64 s[10:11], v94, v150
	s_and_b64 s[8:9], vcc, s[8:9]
	v_subrev_u32_e32 v100, 39, v4
	v_fmac_f32_e32 v92, 0xbfb8aa3b, v184
	s_and_b64 s[10:11], vcc, s[10:11]
	v_cndmask_b32_e64 v93, v93, v165, s[8:9]
	v_cmp_gt_i32_e64 s[8:9], v100, v150
	v_add_u32_e32 v100, -7, v4
	v_cndmask_b32_e64 v92, v92, v165, s[10:11]
	v_fmamk_f32 v95, v95, 0x3fb8aa3b, v170
	v_fmamk_f32 v94, v111, 0x3fb8aa3b, v170
	v_cmp_gt_i32_e64 s[10:11], v100, v150
	v_fmac_f32_e32 v95, 0xbfb8aa3b, v181
	v_fmac_f32_e32 v94, 0xbfb8aa3b, v185
	s_and_b64 s[10:11], vcc, s[10:11]
	s_and_b64 s[8:9], vcc, s[8:9]
	v_cndmask_b32_e64 v94, v94, v165, s[10:11]
	v_cndmask_b32_e64 v95, v95, v165, s[8:9]
	v_max_f32_e32 v99, v93, v92
	v_max_f32_e32 v100, v95, v94
	v_max3_f32 v100, v98, v99, v100
	v_subrev_u32_e32 v99, 38, v4
	v_cmp_gt_i32_e64 s[8:9], v99, v150
	v_add_u32_e32 v99, -6, v4
	v_fmamk_f32 v98, v96, 0x3fb8aa3b, v170
	v_fmamk_f32 v96, v112, 0x3fb8aa3b, v170
	v_cmp_gt_i32_e64 s[10:11], v99, v150
	v_fmac_f32_e32 v98, 0xbfb8aa3b, v182
	v_fmac_f32_e32 v96, 0xbfb8aa3b, v186
	s_and_b64 s[10:11], vcc, s[10:11]
	s_and_b64 s[8:9], vcc, s[8:9]
	v_subrev_u32_e32 v102, 37, v4
	v_add_u32_e32 v4, -5, v4
	v_cndmask_b32_e64 v96, v96, v165, s[10:11]
	v_cndmask_b32_e64 v98, v98, v165, s[8:9]
	v_fmamk_f32 v99, v97, 0x3fb8aa3b, v170
	v_fmamk_f32 v97, v113, 0x3fb8aa3b, v170
	v_cmp_gt_i32_e64 s[8:9], v102, v150
	v_cmp_gt_i32_e64 s[10:11], v4, v150
	v_fmac_f32_e32 v99, 0xbfb8aa3b, v183
	v_fmac_f32_e32 v97, 0xbfb8aa3b, v187
	s_and_b64 s[10:11], vcc, s[10:11]
	s_and_b64 vcc, vcc, s[8:9]
	v_cndmask_b32_e64 v97, v97, v165, s[10:11]
	v_cndmask_b32_e32 v99, v99, v165, vcc
	s_branch .Lfox_join
.Lfox_nomask:
	v_fmac_f32_e32 v6, 0xbfb8aa3b, v12
	s_nop 7
	v_fmamk_f32 v5, v98, 0x3fb8aa3b, v170
	v_cndmask_b32_e32 v2, v7, v2, vcc
	v_fmamk_f32 v7, v99, 0x3fb8aa3b, v170
	v_fmac_f32_e32 v5, 0xbfb8aa3b, v180
	v_fmac_f32_e32 v7, 0xbfb8aa3b, v181
	v_max_f32_e32 v8, v6, v5
	v_max_f32_e32 v9, v2, v7
	v_max3_f32 v12, v8, s45, v9
	v_fmamk_f32 v9, v84, 0x3fb8aa3b, v170
	v_fmac_f32_e32 v9, 0xbfb8aa3b, v14
	v_fmamk_f32 v8, v100, 0x3fb8aa3b, v170
	v_fmac_f32_e32 v8, 0xbfb8aa3b, v182
	v_fmamk_f32 v11, v85, 0x3fb8aa3b, v170
	v_fmamk_f32 v10, v101, 0x3fb8aa3b, v170
	v_fmac_f32_e32 v11, 0xbfb8aa3b, v15
	v_fmac_f32_e32 v10, 0xbfb8aa3b, v183
	v_max_f32_e32 v13, v9, v8
	v_max_f32_e32 v14, v11, v10
	v_max3_f32 v16, v12, v13, v14
	v_fmamk_f32 v13, v86, 0x3fb8aa3b, v170
	v_fmac_f32_e32 v13, 0xbfb8aa3b, v184
	v_fmamk_f32 v12, v102, 0x3fb8aa3b, v170
	v_fmac_f32_e32 v12, 0xbfb8aa3b, v188
	v_fmamk_f32 v15, v87, 0x3fb8aa3b, v170
	v_fmamk_f32 v14, v103, 0x3fb8aa3b, v170
	v_fmac_f32_e32 v15, 0xbfb8aa3b, v185
	v_fmac_f32_e32 v14, 0xbfb8aa3b, v189
	v_max_f32_e32 v17, v13, v12
	v_max_f32_e32 v82, v15, v14
	v_max3_f32 v84, v16, v17, v82
	v_fmamk_f32 v17, v88, 0x3fb8aa3b, v170
	v_fmac_f32_e32 v17, 0xbfb8aa3b, v186
	v_fmamk_f32 v16, v104, 0x3fb8aa3b, v170
	v_fmac_f32_e32 v16, 0xbfb8aa3b, v190
	v_fmamk_f32 v83, v89, 0x3fb8aa3b, v170
	v_fmamk_f32 v82, v105, 0x3fb8aa3b, v170
	v_fmac_f32_e32 v83, 0xbfb8aa3b, v187
	v_fmac_f32_e32 v82, 0xbfb8aa3b, v191
	ds_read_b128 v[98:101], v192 offset:32832
	ds_read_b128 v[180:183], v192 offset:32864
	ds_read_b128 v[102:105], v192 offset:32960
	ds_read_b128 v[184:187], v192 offset:32992
	v_max_f32_e32 v85, v17, v16
	v_max_f32_e32 v86, v83, v82
	v_max3_f32 v87, v84, v85, v86
	v_fmamk_f32 v85, v90, 0x3fb8aa3b, v170
	s_waitcnt lgkmcnt(0)
	v_fmac_f32_e32 v85, 0xbfb8aa3b, v98
	v_fmamk_f32 v84, v106, 0x3fb8aa3b, v170
	v_fmac_f32_e32 v84, 0xbfb8aa3b, v102
	v_fmamk_f32 v88, v91, 0x3fb8aa3b, v170
	v_fmamk_f32 v86, v107, 0x3fb8aa3b, v170
	v_fmac_f32_e32 v88, 0xbfb8aa3b, v99
	v_fmac_f32_e32 v86, 0xbfb8aa3b, v103
	v_max_f32_e32 v89, v85, v84
	v_max_f32_e32 v90, v88, v86
	v_max3_f32 v98, v87, v89, v90
	v_fmamk_f32 v89, v92, 0x3fb8aa3b, v170
	v_fmac_f32_e32 v89, 0xbfb8aa3b, v100
	v_fmamk_f32 v87, v108, 0x3fb8aa3b, v170
	v_fmamk_f32 v91, v93, 0x3fb8aa3b, v170
	v_fmac_f32_e32 v87, 0xbfb8aa3b, v104
	v_fmamk_f32 v90, v109, 0x3fb8aa3b, v170
	v_fmac_f32_e32 v91, 0xbfb8aa3b, v101
	v_fmac_f32_e32 v90, 0xbfb8aa3b, v105
	v_max_f32_e32 v92, v89, v87
	v_max_f32_e32 v93, v91, v90
	v_max3_f32 v98, v98, v92, v93
	v_fmamk_f32 v93, v94, 0x3fb8aa3b, v170
	v_fmac_f32_e32 v93, 0xbfb8aa3b, v180
	v_fmamk_f32 v92, v110, 0x3fb8aa3b, v170
	v_fmac_f32_e32 v92, 0xbfb8aa3b, v184
	v_fmamk_f32 v95, v95, 0x3fb8aa3b, v170
	v_fmamk_f32 v94, v111, 0x3fb8aa3b, v170
	v_fmac_f32_e32 v95, 0xbfb8aa3b, v181
	v_fmac_f32_e32 v94, 0xbfb8aa3b, v185
	v_max_f32_e32 v99, v93, v92
	v_max_f32_e32 v100, v95, v94
	v_max3_f32 v100, v98, v99, v100
	v_fmamk_f32 v98, v96, 0x3fb8aa3b, v170
	v_fmamk_f32 v96, v112, 0x3fb8aa3b, v170
	v_fmac_f32_e32 v98, 0xbfb8aa3b, v182
	v_fmac_f32_e32 v96, 0xbfb8aa3b, v186
	v_subrev_u32_e32 v102, 37, v4
	v_fmamk_f32 v99, v97, 0x3fb8aa3b, v170
	v_fmamk_f32 v97, v113, 0x3fb8aa3b, v170
	v_fmac_f32_e32 v99, 0xbfb8aa3b, v183
	v_fmac_f32_e32 v97, 0xbfb8aa3b, v187
.Lfox_join:
	v_max_f32_e32 v101, v98, v96
	v_max_f32_e32 v4, v99, v97
	v_max3_f32 v4, v100, v101, v4
	v_mov_b32_e32 v100, v4
	s_nop 1
	v_permlane32_swap_b32_e32 v4, v100
	v_max_f32_e32 v100, v100, v100
	v_max_f32_e32 v4, v4, v4
	v_max_f32_e32 v4, v4, v100
	v_sub_f32_e32 v100, v4, v179
	v_cmp_ge_f32_e32 vcc, s46, v100
	s_cmp_eq_u64 vcc, exec
	v_mov_b32_e32 v100, 1.0
	s_cbranch_scc1 .LBB0_657
	v_max_f32_e32 v4, v4, v4
	v_max_f32_e32 v100, v179, v179
	v_max_f32_e32 v4, v100, v4
	v_sub_f32_e32 v100, v179, v4
	v_exp_f32_e32 v100, v100
	s_and_saveexec_b64 s[8:9], s[6:7]
	ds_write_b32 v169, v100
	s_or_b64 exec, exec, s[8:9]
	s_waitcnt lgkmcnt(0)
	v_add_u32_e32 v101, s55, v148
	ds_read_b128 v[102:105], v101 offset:96
	ds_read_b128 v[106:109], v101 offset:64
	ds_read_b128 v[110:113], v101 offset:32
	ds_read_b128 v[180:183], v101
	s_waitcnt lgkmcnt(0)
	v_pk_mul_f32 v[78:79], v[78:79], v[102:103]
	v_pk_mul_f32 v[74:75], v[74:75], v[106:107]
	v_pk_mul_f32 v[70:71], v[70:71], v[110:111]
	v_pk_mul_f32 v[80:81], v[80:81], v[104:105]
	v_pk_mul_f32 v[76:77], v[76:77], v[108:109]
	v_pk_mul_f32 v[72:73], v[72:73], v[112:113]
	v_pk_mul_f32 v[68:69], v[68:69], v[182:183]
	v_pk_mul_f32 v[66:67], v[66:67], v[180:181]
	v_pk_mul_f32 v[62:63], v[62:63], v[102:103]
	v_pk_mul_f32 v[58:59], v[58:59], v[106:107]
	v_pk_mul_f32 v[54:55], v[54:55], v[110:111]
	v_pk_mul_f32 v[64:65], v[64:65], v[104:105]
	v_pk_mul_f32 v[60:61], v[60:61], v[108:109]
	v_pk_mul_f32 v[56:57], v[56:57], v[112:113]
	v_pk_mul_f32 v[52:53], v[52:53], v[182:183]
	v_pk_mul_f32 v[50:51], v[50:51], v[180:181]
	v_pk_mul_f32 v[46:47], v[46:47], v[102:103]
	v_pk_mul_f32 v[42:43], v[42:43], v[106:107]
	v_pk_mul_f32 v[38:39], v[38:39], v[110:111]
	v_pk_mul_f32 v[48:49], v[48:49], v[104:105]
	v_pk_mul_f32 v[44:45], v[44:45], v[108:109]
	v_pk_mul_f32 v[40:41], v[40:41], v[112:113]
	v_pk_mul_f32 v[36:37], v[36:37], v[182:183]
	v_pk_mul_f32 v[34:35], v[34:35], v[180:181]
	v_pk_mul_f32 v[30:31], v[30:31], v[102:103]
	v_pk_mul_f32 v[26:27], v[26:27], v[106:107]
	v_pk_mul_f32 v[22:23], v[22:23], v[110:111]
	v_pk_mul_f32 v[32:33], v[32:33], v[104:105]
	v_pk_mul_f32 v[28:29], v[28:29], v[108:109]
	v_pk_mul_f32 v[24:25], v[24:25], v[112:113]
	v_pk_mul_f32 v[20:21], v[20:21], v[182:183]
	v_pk_mul_f32 v[18:19], v[18:19], v[180:181]
	s_branch .LBB0_658
